# layer1: low four W fragments of MFMA steps 0-3 double-buffered through the idle SELF registers
# speedup vs baseline: 1.0011x; 1.0005x over previous
.Lg1_final:
	v_max_i32_e32 v94, 1, v78
	v_cvt_f32_u32_e32 v94, v94
	v_div_scale_f32 v96, s[62:63], v94, v94, 1.0
	v_rcp_f32_e32 v97, v96
	v_div_scale_f32 v98, vcc, 1.0, v94, 1.0
	v_fma_f32 v99, -v96, v97, 1.0
	v_fmac_f32_e32 v97, v99, v97
	v_mul_f32_e32 v99, v98, v97
	v_fma_f32 v95, -v96, v99, v98
	v_fmac_f32_e32 v99, v95, v97
	v_fma_f32 v96, -v96, v99, v98
	v_div_fmas_f32 v96, v96, v97, v99
	v_div_fixup_f32 v95, v96, v94, 1.0
	v_mul_f32_e32 v18, 0x43000000, v18
	v_sub_f32_e32 v2, v2, v18
	v_sub_f32_e32 v3, v3, v18
	v_sub_f32_e32 v4, v4, v18
	v_sub_f32_e32 v5, v5, v18
	v_sub_f32_e32 v6, v6, v18
	v_sub_f32_e32 v7, v7, v18
	v_sub_f32_e32 v8, v8, v18
	v_sub_f32_e32 v9, v9, v18
	v_sub_f32_e32 v10, v10, v18
	v_sub_f32_e32 v11, v11, v18
	v_sub_f32_e32 v12, v12, v18
	v_sub_f32_e32 v13, v13, v18
	v_sub_f32_e32 v14, v14, v18
	v_sub_f32_e32 v15, v15, v18
	v_sub_f32_e32 v16, v16, v18
	v_sub_f32_e32 v17, v17, v18
	v_mul_f32_e32 v2, v95, v2
	v_mul_f32_e32 v3, v95, v3
	v_mul_f32_e32 v4, v95, v4
	v_mul_f32_e32 v5, v95, v5
	v_mul_f32_e32 v6, v95, v6
	v_mul_f32_e32 v7, v95, v7
	v_mul_f32_e32 v8, v95, v8
	v_mul_f32_e32 v9, v95, v9
	v_mul_f32_e32 v10, v95, v10
	v_mul_f32_e32 v11, v95, v11
	v_mul_f32_e32 v12, v95, v12
	v_mul_f32_e32 v13, v95, v13
	v_mul_f32_e32 v14, v95, v14
	v_mul_f32_e32 v15, v95, v15
	v_mul_f32_e32 v16, v95, v16
	v_mul_f32_e32 v17, v95, v17
	v_cvt_pk_f16_f32 v52, v2, v3
	v_cvt_pk_f16_f32 v53, v4, v5
	v_cvt_pk_f16_f32 v54, v6, v7
	v_cvt_pk_f16_f32 v55, v8, v9
	v_cvt_pk_f16_f32 v56, v10, v11
	v_cvt_pk_f16_f32 v57, v12, v13
	v_cvt_pk_f16_f32 v58, v14, v15
	v_cvt_pk_f16_f32 v59, v16, v17
	ds_write_b128 v93, v[52:55]
	ds_write_b128 v93, v[56:59] offset:16
	s_add_u32 s39, s39, 1
	s_cmp_lt_u32 s39, 2
	s_cbranch_scc1 .Lg1_set_top
	v_lshlrev_b32_e32 v107, 9, v105
	v_xor_b32_e32 v108, v106, v105
	v_lshlrev_b32_e32 v108, 4, v108
	v_mul_u32_u24_e32 v109, 0x110, v105
	v_lshl_add_u32 v109, v106, 4, v109
	v_add_u32_e32 v109, s48, v109
	v_lshlrev_b32_e32 v110, 4, v106
	v_add_u32_e32 v110, 0x10000, v110
	s_waitcnt lgkmcnt(0)
	ds_read_b128 v[52:55], v110 offset:0
	ds_read_b128 v[56:59], v110 offset:64
	ds_read_b128 v[60:63], v110 offset:128
	ds_read_b128 v[64:67], v110 offset:192
	ds_read_b128 v[68:71], v110 offset:256
	ds_read_b128 v[72:75], v110 offset:320
	ds_read_b128 v[76:79], v110 offset:384
	ds_read_b128 v[80:83], v110 offset:448
	v_xor_b32_e32 v111, 0, v108
	v_add_u32_e32 v111, v111, v107
	ds_read_b128 v[16:19], v109 offset:0
	ds_read_b128 v[84:87], v111 offset:0
	ds_read_b128 v[88:91], v111 offset:8192
	ds_read_b128 v[92:95], v111 offset:16384
	ds_read_b128 v[96:99], v111 offset:24576
	ds_read_b128 v[0:3], v111 offset:32768
	ds_read_b128 v[4:7], v111 offset:40960
	ds_read_b128 v[8:11], v111 offset:49152
	ds_read_b128 v[12:15], v111 offset:57344
	s_waitcnt lgkmcnt(0)
	v_xor_b32_e32 v111, 64, v108
	v_add_u32_e32 v111, v111, v107
	ds_read_b128 v[112:115], v111 offset:0
	ds_read_b128 v[116:119], v111 offset:8192
	ds_read_b128 v[120:123], v111 offset:16384
	ds_read_b128 v[124:127], v111 offset:24576
	v_mfma_f32_16x16x32_f16 v[52:55], v[84:87], v[16:19], v[52:55]
	v_mfma_f32_16x16x32_f16 v[56:59], v[88:91], v[16:19], v[56:59]
	v_mfma_f32_16x16x32_f16 v[60:63], v[92:95], v[16:19], v[60:63]
	v_mfma_f32_16x16x32_f16 v[64:67], v[96:99], v[16:19], v[64:67]
	v_mfma_f32_16x16x32_f16 v[68:71], v[0:3], v[16:19], v[68:71]
	v_mfma_f32_16x16x32_f16 v[72:75], v[4:7], v[16:19], v[72:75]
	v_mfma_f32_16x16x32_f16 v[76:79], v[8:11], v[16:19], v[76:79]
	v_mfma_f32_16x16x32_f16 v[80:83], v[12:15], v[16:19], v[80:83]
	v_xor_b32_e32 v111, 64, v108
	v_add_u32_e32 v111, v111, v107
	ds_read_b128 v[100:103], v109 offset:64
	ds_read_b128 v[0:3], v111 offset:32768
	ds_read_b128 v[4:7], v111 offset:40960
	ds_read_b128 v[8:11], v111 offset:49152
	ds_read_b128 v[12:15], v111 offset:57344
	s_waitcnt lgkmcnt(0)
	v_xor_b32_e32 v111, 128, v108
	v_add_u32_e32 v111, v111, v107
	ds_read_b128 v[84:87], v111 offset:0
	ds_read_b128 v[88:91], v111 offset:8192
	ds_read_b128 v[92:95], v111 offset:16384
	ds_read_b128 v[96:99], v111 offset:24576
	v_mfma_f32_16x16x32_f16 v[52:55], v[112:115], v[100:103], v[52:55]
	v_mfma_f32_16x16x32_f16 v[56:59], v[116:119], v[100:103], v[56:59]
	v_mfma_f32_16x16x32_f16 v[60:63], v[120:123], v[100:103], v[60:63]
	v_mfma_f32_16x16x32_f16 v[64:67], v[124:127], v[100:103], v[64:67]
	v_mfma_f32_16x16x32_f16 v[68:71], v[0:3], v[100:103], v[68:71]
	v_mfma_f32_16x16x32_f16 v[72:75], v[4:7], v[100:103], v[72:75]
	v_mfma_f32_16x16x32_f16 v[76:79], v[8:11], v[100:103], v[76:79]
	v_mfma_f32_16x16x32_f16 v[80:83], v[12:15], v[100:103], v[80:83]
	v_xor_b32_e32 v111, 128, v108
	v_add_u32_e32 v111, v111, v107
	ds_read_b128 v[16:19], v109 offset:128
	ds_read_b128 v[0:3], v111 offset:32768
	ds_read_b128 v[4:7], v111 offset:40960
	ds_read_b128 v[8:11], v111 offset:49152
	ds_read_b128 v[12:15], v111 offset:57344
	s_waitcnt lgkmcnt(0)
	v_xor_b32_e32 v111, 192, v108
	v_add_u32_e32 v111, v111, v107
	ds_read_b128 v[112:115], v111 offset:0
	ds_read_b128 v[116:119], v111 offset:8192
	ds_read_b128 v[120:123], v111 offset:16384
	ds_read_b128 v[124:127], v111 offset:24576
	v_mfma_f32_16x16x32_f16 v[52:55], v[84:87], v[16:19], v[52:55]
	v_mfma_f32_16x16x32_f16 v[56:59], v[88:91], v[16:19], v[56:59]
	v_mfma_f32_16x16x32_f16 v[60:63], v[92:95], v[16:19], v[60:63]
	v_mfma_f32_16x16x32_f16 v[64:67], v[96:99], v[16:19], v[64:67]
	v_mfma_f32_16x16x32_f16 v[68:71], v[0:3], v[16:19], v[68:71]
	v_mfma_f32_16x16x32_f16 v[72:75], v[4:7], v[16:19], v[72:75]
	v_mfma_f32_16x16x32_f16 v[76:79], v[8:11], v[16:19], v[76:79]
	v_mfma_f32_16x16x32_f16 v[80:83], v[12:15], v[16:19], v[80:83]
	v_xor_b32_e32 v111, 192, v108
	v_add_u32_e32 v111, v111, v107
	ds_read_b128 v[100:103], v109 offset:192
	ds_read_b128 v[0:3], v111 offset:32768
	ds_read_b128 v[4:7], v111 offset:40960
	ds_read_b128 v[8:11], v111 offset:49152
	ds_read_b128 v[12:15], v111 offset:57344
	s_waitcnt lgkmcnt(0)
	v_mfma_f32_16x16x32_f16 v[52:55], v[112:115], v[100:103], v[52:55]
	v_mfma_f32_16x16x32_f16 v[56:59], v[116:119], v[100:103], v[56:59]
	v_mfma_f32_16x16x32_f16 v[60:63], v[120:123], v[100:103], v[60:63]
	v_mfma_f32_16x16x32_f16 v[64:67], v[124:127], v[100:103], v[64:67]
	v_mfma_f32_16x16x32_f16 v[68:71], v[0:3], v[100:103], v[68:71]
	v_mfma_f32_16x16x32_f16 v[72:75], v[4:7], v[100:103], v[72:75]
	v_mfma_f32_16x16x32_f16 v[76:79], v[8:11], v[100:103], v[76:79]
	v_mfma_f32_16x16x32_f16 v[80:83], v[12:15], v[100:103], v[80:83]
	s_waitcnt vmcnt(0)
	v_cvt_pk_f16_f32 v112, v20, v21
	v_cvt_pk_f16_f32 v113, v22, v23
	v_cvt_pk_f16_f32 v114, v24, v25
	v_cvt_pk_f16_f32 v115, v26, v27
	v_cvt_pk_f16_f32 v116, v28, v29
	v_cvt_pk_f16_f32 v117, v30, v31
	v_cvt_pk_f16_f32 v118, v32, v33
	v_cvt_pk_f16_f32 v119, v34, v35
	v_cvt_pk_f16_f32 v120, v36, v37
	v_cvt_pk_f16_f32 v121, v38, v39
	v_cvt_pk_f16_f32 v122, v40, v41
	v_cvt_pk_f16_f32 v123, v42, v43
	v_cvt_pk_f16_f32 v124, v44, v45
	v_cvt_pk_f16_f32 v125, v46, v47
	v_cvt_pk_f16_f32 v126, v48, v49
	v_cvt_pk_f16_f32 v127, v50, v51
	v_xor_b32_e32 v111, 256, v108
	v_add_u32_e32 v111, v111, v107
	ds_read_b128 v[84:87], v111 offset:0
	ds_read_b128 v[88:91], v111 offset:8192
	ds_read_b128 v[92:95], v111 offset:16384
	ds_read_b128 v[96:99], v111 offset:24576
	ds_read_b128 v[0:3], v111 offset:32768
	ds_read_b128 v[4:7], v111 offset:40960
	ds_read_b128 v[8:11], v111 offset:49152
	ds_read_b128 v[12:15], v111 offset:57344
	s_waitcnt lgkmcnt(0)
	v_xor_b32_e32 v111, 320, v108
	v_add_u32_e32 v111, v111, v107
	ds_read_b128 v[20:23], v111 offset:0
	ds_read_b128 v[24:27], v111 offset:8192
	ds_read_b128 v[28:31], v111 offset:16384
	ds_read_b128 v[32:35], v111 offset:24576
	ds_read_b128 v[36:39], v111 offset:32768
	ds_read_b128 v[40:43], v111 offset:40960
	ds_read_b128 v[44:47], v111 offset:49152
	ds_read_b128 v[48:51], v111 offset:57344
	v_mfma_f32_16x16x32_f16 v[52:55], v[84:87], v[112:115], v[52:55]
	v_mfma_f32_16x16x32_f16 v[56:59], v[88:91], v[112:115], v[56:59]
	v_mfma_f32_16x16x32_f16 v[60:63], v[92:95], v[112:115], v[60:63]
	v_mfma_f32_16x16x32_f16 v[64:67], v[96:99], v[112:115], v[64:67]
	v_mfma_f32_16x16x32_f16 v[68:71], v[0:3], v[112:115], v[68:71]
	v_mfma_f32_16x16x32_f16 v[72:75], v[4:7], v[112:115], v[72:75]
	v_mfma_f32_16x16x32_f16 v[76:79], v[8:11], v[112:115], v[76:79]
	v_mfma_f32_16x16x32_f16 v[80:83], v[12:15], v[112:115], v[80:83]
	s_waitcnt lgkmcnt(0)
	v_xor_b32_e32 v111, 384, v108
	v_add_u32_e32 v111, v111, v107
	ds_read_b128 v[84:87], v111 offset:0
	ds_read_b128 v[88:91], v111 offset:8192
	ds_read_b128 v[92:95], v111 offset:16384
	ds_read_b128 v[96:99], v111 offset:24576
	ds_read_b128 v[0:3], v111 offset:32768
	ds_read_b128 v[4:7], v111 offset:40960
	ds_read_b128 v[8:11], v111 offset:49152
	ds_read_b128 v[12:15], v111 offset:57344
	v_mfma_f32_16x16x32_f16 v[52:55], v[20:23], v[116:119], v[52:55]
	v_mfma_f32_16x16x32_f16 v[56:59], v[24:27], v[116:119], v[56:59]
	v_mfma_f32_16x16x32_f16 v[60:63], v[28:31], v[116:119], v[60:63]
	v_mfma_f32_16x16x32_f16 v[64:67], v[32:35], v[116:119], v[64:67]
	v_mfma_f32_16x16x32_f16 v[68:71], v[36:39], v[116:119], v[68:71]
	v_mfma_f32_16x16x32_f16 v[72:75], v[40:43], v[116:119], v[72:75]
	v_mfma_f32_16x16x32_f16 v[76:79], v[44:47], v[116:119], v[76:79]
	v_mfma_f32_16x16x32_f16 v[80:83], v[48:51], v[116:119], v[80:83]
	s_waitcnt lgkmcnt(0)
	v_xor_b32_e32 v111, 448, v108
	v_add_u32_e32 v111, v111, v107
	ds_read_b128 v[20:23], v111 offset:0
	ds_read_b128 v[24:27], v111 offset:8192
	ds_read_b128 v[28:31], v111 offset:16384
	ds_read_b128 v[32:35], v111 offset:24576
	ds_read_b128 v[36:39], v111 offset:32768
	ds_read_b128 v[40:43], v111 offset:40960
	ds_read_b128 v[44:47], v111 offset:49152
	ds_read_b128 v[48:51], v111 offset:57344
	v_mfma_f32_16x16x32_f16 v[52:55], v[84:87], v[120:123], v[52:55]
	v_mfma_f32_16x16x32_f16 v[56:59], v[88:91], v[120:123], v[56:59]
	v_mfma_f32_16x16x32_f16 v[60:63], v[92:95], v[120:123], v[60:63]
	v_mfma_f32_16x16x32_f16 v[64:67], v[96:99], v[120:123], v[64:67]
	v_mfma_f32_16x16x32_f16 v[68:71], v[0:3], v[120:123], v[68:71]
	v_mfma_f32_16x16x32_f16 v[72:75], v[4:7], v[120:123], v[72:75]
	v_mfma_f32_16x16x32_f16 v[76:79], v[8:11], v[120:123], v[76:79]
	v_mfma_f32_16x16x32_f16 v[80:83], v[12:15], v[120:123], v[80:83]
	s_waitcnt lgkmcnt(0)
	v_mfma_f32_16x16x32_f16 v[52:55], v[20:23], v[124:127], v[52:55]
	v_mfma_f32_16x16x32_f16 v[56:59], v[24:27], v[124:127], v[56:59]
	v_mfma_f32_16x16x32_f16 v[60:63], v[28:31], v[124:127], v[60:63]
	v_mfma_f32_16x16x32_f16 v[64:67], v[32:35], v[124:127], v[64:67]
	v_mfma_f32_16x16x32_f16 v[68:71], v[36:39], v[124:127], v[68:71]
	v_mfma_f32_16x16x32_f16 v[72:75], v[40:43], v[124:127], v[72:75]
	v_mfma_f32_16x16x32_f16 v[76:79], v[44:47], v[124:127], v[76:79]
	v_mfma_f32_16x16x32_f16 v[80:83], v[48:51], v[124:127], v[80:83]
	s_nop 7
	s_nop 3
	v_max_f32_e32 v52, 0, v52
	v_max_f32_e32 v53, 0, v53
	v_max_f32_e32 v54, 0, v54
	v_max_f32_e32 v55, 0, v55
	v_max_f32_e32 v56, 0, v56
	v_max_f32_e32 v57, 0, v57
	v_max_f32_e32 v58, 0, v58
	v_max_f32_e32 v59, 0, v59
	v_max_f32_e32 v60, 0, v60
	v_max_f32_e32 v61, 0, v61
	v_max_f32_e32 v62, 0, v62
	v_max_f32_e32 v63, 0, v63
	v_max_f32_e32 v64, 0, v64
	v_max_f32_e32 v65, 0, v65
	v_max_f32_e32 v66, 0, v66
	v_max_f32_e32 v67, 0, v67
	v_max_f32_e32 v68, 0, v68
	v_max_f32_e32 v69, 0, v69
	v_max_f32_e32 v70, 0, v70
	v_max_f32_e32 v71, 0, v71
	v_max_f32_e32 v72, 0, v72
	v_max_f32_e32 v73, 0, v73
	v_max_f32_e32 v74, 0, v74
	v_max_f32_e32 v75, 0, v75
	v_max_f32_e32 v76, 0, v76
	v_max_f32_e32 v77, 0, v77
	v_max_f32_e32 v78, 0, v78
	v_max_f32_e32 v79, 0, v79
	v_max_f32_e32 v80, 0, v80
	v_max_f32_e32 v81, 0, v81
	v_max_f32_e32 v82, 0, v82
	v_max_f32_e32 v83, 0, v83
	v_max3_f32 v1, v52, v53, v54
	v_max3_f32 v1, v1, v55, v56
	v_max3_f32 v1, v1, v57, v58
	v_max3_f32 v1, v1, v59, v60
	v_max3_f32 v1, v1, v61, v62
	v_max3_f32 v1, v1, v63, v64
	v_max3_f32 v1, v1, v65, v66
	v_max3_f32 v1, v1, v67, v68
	v_max3_f32 v1, v1, v69, v70
	v_max3_f32 v1, v1, v71, v72
	v_max3_f32 v1, v1, v73, v74
	v_max3_f32 v1, v1, v75, v76
	v_max3_f32 v1, v1, v77, v78
	v_max3_f32 v1, v1, v79, v80
	v_max3_f32 v1, v1, v81, v82
	v_max_f32_e32 v1, v1, v83
	v_lshl_or_b32 v0, v106, 4, v105
	v_xor_b32_e32 v2, 16, v0
	v_lshlrev_b32_e32 v2, 2, v2
	ds_bpermute_b32 v3, v2, v1
	s_waitcnt lgkmcnt(0)
	v_max_f32_e32 v1, v1, v3
	v_xor_b32_e32 v2, 32, v0
	v_lshlrev_b32_e32 v2, 2, v2
	ds_bpermute_b32 v3, v2, v1
	s_waitcnt lgkmcnt(0)
	v_max_f32_e32 v1, v1, v3
	s_mov_b32 s58, 0x437f0000
	v_div_scale_f32 v5, s[62:63], v1, v1, s58
	v_rcp_f32_e32 v6, v5
	v_div_scale_f32 v7, vcc, s58, v1, s58
	v_fma_f32 v8, -v5, v6, 1.0
	v_fmac_f32_e32 v6, v8, v6
	v_mul_f32_e32 v8, v7, v6
	v_fma_f32 v4, -v5, v8, v7
	v_fmac_f32_e32 v8, v4, v6
	v_fma_f32 v5, -v5, v8, v7
	v_div_fmas_f32 v5, v5, v6, v8
	v_div_fixup_f32 v4, v5, v1, s58
	v_cmp_lt_f32_e32 vcc, 0, v1
	s_nop 1
	v_cndmask_b32_e32 v4, 0, v4, vcc
	v_mul_u32_u24_e32 v9, 0x110, v105
	v_lshl_add_u32 v9, v106, 3, v9
	v_add_u32_e32 v9, s48, v9
	v_mul_u32_u24_e32 v10, 0x110, v106
	v_lshl_add_u32 v10, v105, 4, v10
	v_add_u32_e32 v10, s48, v10
	v_mul_u32_u24_e32 v11, 0x90, v105
	v_lshl_add_u32 v11, v106, 2, v11
	v_add_u32_e32 v11, s48, v11
	v_lshrrev_b32_e32 v14, 3, v0
	v_and_b32_e32 v16, 7, v0
	v_mul_u32_u24_e32 v12, 0x90, v14
	v_lshl_add_u32 v12, v16, 4, v12
	v_add_u32_e32 v12, s48, v12
	v_lshlrev_b32_e32 v14, 2, v14
	v_lshlrev_b32_e32 v16, 4, v16
	v_lshlrev_b32_e32 v13, 2, v106
	v_lshlrev_b32_e32 v15, 4, v105
	ds_bpermute_b32 v20, v13, v104 offset:0
	ds_bpermute_b32 v21, v13, v104 offset:16
	ds_bpermute_b32 v22, v13, v104 offset:32
	ds_bpermute_b32 v23, v13, v104 offset:48
	ds_bpermute_b32 v24, v14, v104 offset:0
	ds_bpermute_b32 v25, v14, v104 offset:32
	s_waitcnt lgkmcnt(0)
	v_cvt_pk_f16_f32 v26, v52, v53
	v_cvt_pk_f16_f32 v27, v54, v55
	ds_write_b64 v9, v[26:27] offset:0
	v_cvt_pk_f16_f32 v26, v56, v57
	v_cvt_pk_f16_f32 v27, v58, v59
	ds_write_b64 v9, v[26:27] offset:32
	v_cvt_pk_f16_f32 v26, v60, v61
	v_cvt_pk_f16_f32 v27, v62, v63
	ds_write_b64 v9, v[26:27] offset:64
	v_cvt_pk_f16_f32 v26, v64, v65
	v_cvt_pk_f16_f32 v27, v66, v67
	ds_write_b64 v9, v[26:27] offset:96
	v_cvt_pk_f16_f32 v26, v68, v69
	v_cvt_pk_f16_f32 v27, v70, v71
	ds_write_b64 v9, v[26:27] offset:128
	v_cvt_pk_f16_f32 v26, v72, v73
	v_cvt_pk_f16_f32 v27, v74, v75
	ds_write_b64 v9, v[26:27] offset:160
	v_cvt_pk_f16_f32 v26, v76, v77
	v_cvt_pk_f16_f32 v27, v78, v79
	ds_write_b64 v9, v[26:27] offset:192
	v_cvt_pk_f16_f32 v26, v80, v81
	v_cvt_pk_f16_f32 v27, v82, v83
	ds_write_b64 v9, v[26:27] offset:224
	ds_read_b128 v[28:31], v10 offset:0
	ds_read_b128 v[32:35], v10 offset:1088
	ds_read_b128 v[36:39], v10 offset:2176
	ds_read_b128 v[40:43], v10 offset:3264
	s_waitcnt lgkmcnt(3)
	v_lshl_or_b32 v20, v20, 8, v15
	global_store_dwordx4 v20, v[28:31], s[26:27] sc1
	s_waitcnt lgkmcnt(2)
	v_lshl_or_b32 v21, v21, 8, v15
	global_store_dwordx4 v21, v[32:35], s[26:27] sc1
	s_waitcnt lgkmcnt(1)
	v_lshl_or_b32 v22, v22, 8, v15
	global_store_dwordx4 v22, v[36:39], s[26:27] sc1
	s_waitcnt lgkmcnt(0)
	v_lshl_or_b32 v23, v23, 8, v15
	global_store_dwordx4 v23, v[40:43], s[26:27] sc1
	v_mul_f32_e32 v44, v4, v52
	v_mul_f32_e32 v45, v4, v53
	v_mul_f32_e32 v46, v4, v54
	v_mul_f32_e32 v47, v4, v55
	v_rndne_f32_e32 v44, v44
	v_rndne_f32_e32 v45, v45
	v_rndne_f32_e32 v46, v46
	v_rndne_f32_e32 v47, v47
	v_cvt_i32_f32_e32 v44, v44
	v_cvt_i32_f32_e32 v45, v45
	v_cvt_i32_f32_e32 v46, v46
	v_cvt_i32_f32_e32 v47, v47
	v_lshl_or_b32 v44, v45, 8, v44
	v_lshl_or_b32 v44, v46, 16, v44
	v_lshl_or_b32 v44, v47, 24, v44
	ds_write_b32 v11, v44 offset:0
	v_mul_f32_e32 v44, v4, v56
	v_mul_f32_e32 v45, v4, v57
	v_mul_f32_e32 v46, v4, v58
	v_mul_f32_e32 v47, v4, v59
	v_rndne_f32_e32 v44, v44
	v_rndne_f32_e32 v45, v45
	v_rndne_f32_e32 v46, v46
	v_rndne_f32_e32 v47, v47
	v_cvt_i32_f32_e32 v44, v44
	v_cvt_i32_f32_e32 v45, v45
	v_cvt_i32_f32_e32 v46, v46
	v_cvt_i32_f32_e32 v47, v47
	v_lshl_or_b32 v44, v45, 8, v44
	v_lshl_or_b32 v44, v46, 16, v44
	v_lshl_or_b32 v44, v47, 24, v44
	ds_write_b32 v11, v44 offset:16
	v_mul_f32_e32 v44, v4, v60
	v_mul_f32_e32 v45, v4, v61
	v_mul_f32_e32 v46, v4, v62
	v_mul_f32_e32 v47, v4, v63
	v_rndne_f32_e32 v44, v44
	v_rndne_f32_e32 v45, v45
	v_rndne_f32_e32 v46, v46
	v_rndne_f32_e32 v47, v47
	v_cvt_i32_f32_e32 v44, v44
	v_cvt_i32_f32_e32 v45, v45
	v_cvt_i32_f32_e32 v46, v46
	v_cvt_i32_f32_e32 v47, v47
	v_lshl_or_b32 v44, v45, 8, v44
	v_lshl_or_b32 v44, v46, 16, v44
	v_lshl_or_b32 v44, v47, 24, v44
	ds_write_b32 v11, v44 offset:32
	v_mul_f32_e32 v44, v4, v64
	v_mul_f32_e32 v45, v4, v65
	v_mul_f32_e32 v46, v4, v66
	v_mul_f32_e32 v47, v4, v67
	v_rndne_f32_e32 v44, v44
	v_rndne_f32_e32 v45, v45
	v_rndne_f32_e32 v46, v46
	v_rndne_f32_e32 v47, v47
	v_cvt_i32_f32_e32 v44, v44
	v_cvt_i32_f32_e32 v45, v45
	v_cvt_i32_f32_e32 v46, v46
	v_cvt_i32_f32_e32 v47, v47
	v_lshl_or_b32 v44, v45, 8, v44
	v_lshl_or_b32 v44, v46, 16, v44
	v_lshl_or_b32 v44, v47, 24, v44
	ds_write_b32 v11, v44 offset:48
	v_mul_f32_e32 v44, v4, v68
	v_mul_f32_e32 v45, v4, v69
	v_mul_f32_e32 v46, v4, v70
	v_mul_f32_e32 v47, v4, v71
	v_rndne_f32_e32 v44, v44
	v_rndne_f32_e32 v45, v45
	v_rndne_f32_e32 v46, v46
	v_rndne_f32_e32 v47, v47
	v_cvt_i32_f32_e32 v44, v44
	v_cvt_i32_f32_e32 v45, v45
	v_cvt_i32_f32_e32 v46, v46
	v_cvt_i32_f32_e32 v47, v47
	v_lshl_or_b32 v44, v45, 8, v44
	v_lshl_or_b32 v44, v46, 16, v44
	v_lshl_or_b32 v44, v47, 24, v44
	ds_write_b32 v11, v44 offset:64
	v_mul_f32_e32 v44, v4, v72
	v_mul_f32_e32 v45, v4, v73
	v_mul_f32_e32 v46, v4, v74
	v_mul_f32_e32 v47, v4, v75
	v_rndne_f32_e32 v44, v44
	v_rndne_f32_e32 v45, v45
	v_rndne_f32_e32 v46, v46
	v_rndne_f32_e32 v47, v47
	v_cvt_i32_f32_e32 v44, v44
	v_cvt_i32_f32_e32 v45, v45
	v_cvt_i32_f32_e32 v46, v46
	v_cvt_i32_f32_e32 v47, v47
	v_lshl_or_b32 v44, v45, 8, v44
	v_lshl_or_b32 v44, v46, 16, v44
	v_lshl_or_b32 v44, v47, 24, v44
	ds_write_b32 v11, v44 offset:80
	v_mul_f32_e32 v44, v4, v76
	v_mul_f32_e32 v45, v4, v77
	v_mul_f32_e32 v46, v4, v78
	v_mul_f32_e32 v47, v4, v79
	v_rndne_f32_e32 v44, v44
	v_rndne_f32_e32 v45, v45
	v_rndne_f32_e32 v46, v46
	v_rndne_f32_e32 v47, v47
	v_cvt_i32_f32_e32 v44, v44
	v_cvt_i32_f32_e32 v45, v45
	v_cvt_i32_f32_e32 v46, v46
	v_cvt_i32_f32_e32 v47, v47
	v_lshl_or_b32 v44, v45, 8, v44
	v_lshl_or_b32 v44, v46, 16, v44
	v_lshl_or_b32 v44, v47, 24, v44
	ds_write_b32 v11, v44 offset:96
	v_mul_f32_e32 v44, v4, v80
	v_mul_f32_e32 v45, v4, v81
	v_mul_f32_e32 v46, v4, v82
	v_mul_f32_e32 v47, v4, v83
	v_rndne_f32_e32 v44, v44
	v_rndne_f32_e32 v45, v45
	v_rndne_f32_e32 v46, v46
	v_rndne_f32_e32 v47, v47
	v_cvt_i32_f32_e32 v44, v44
	v_cvt_i32_f32_e32 v45, v45
	v_cvt_i32_f32_e32 v46, v46
	v_cvt_i32_f32_e32 v47, v47
	v_lshl_or_b32 v44, v45, 8, v44
	v_lshl_or_b32 v44, v46, 16, v44
	v_lshl_or_b32 v44, v47, 24, v44
	ds_write_b32 v11, v44 offset:112
	ds_read_b128 v[84:87], v12 offset:0
	ds_read_b128 v[88:91], v12 offset:1152
	s_waitcnt lgkmcnt(1)
	v_lshl_or_b32 v24, v24, 7, v16
	global_store_dwordx4 v24, v[84:87], s[28:29] sc1
	s_waitcnt lgkmcnt(0)
	v_lshl_or_b32 v25, v25, 7, v16
	global_store_dwordx4 v25, v[88:91], s[28:29] sc1
	v_cmp_eq_u32_e32 vcc, 0, v106
	s_and_saveexec_b64 s[44:45], vcc
	s_mov_b32 s58, 0x3b808081
	v_fma_mixlo_f16 v2, v1, s58, 0
	v_lshlrev_b32_e32 v3, 1, v104
	global_store_short v3, v2, s[30:31]
	s_endpgm
	.p2alignl 8, 3212836864
